# stream: chunk order within a row rotated by XCD id (blk&3) on top of rotated wave-row assignment
# baseline (speedup 1.0000x reference)
.LBB1_2:
	s_or_b64 exec, exec, s[0:1]
	s_lshr_b32 s8, s3, 6
	s_add_i32 s8, s8, s2
	s_and_b32 s8, s8, 15
	s_lshl_b32 s0, s2, 7
	v_and_b32_e32 v24, 63, v0
	s_add_i32 s9, s8, s0
	s_waitcnt lgkmcnt(0)
	s_and_b32 s1, s5, 0xffff
	s_mov_b32 s3, 0x20000
	s_brev_b32 s2, 16
	s_mov_b32 s0, s4
	v_lshlrev_b32_e32 v25, 4, v24
	s_lshr_b32 s11, s9, 7
	s_and_b32 s11, s11, 3
	s_add_i32 s12, s11, 0
	s_and_b32 s12, s12, 3
	s_lshl_b32 s12, s12, 10
	v_add_u32_e32 v67, s12, v25
	s_add_i32 s12, s11, 1
	s_and_b32 s12, s12, 3
	s_lshl_b32 s12, s12, 10
	v_add_u32_e32 v68, s12, v25
	s_add_i32 s12, s11, 2
	s_and_b32 s12, s12, 3
	s_lshl_b32 s12, s12, 10
	v_add_u32_e32 v69, s12, v25
	s_add_i32 s12, s11, 3
	s_and_b32 s12, s12, 3
	s_lshl_b32 s12, s12, 10
	v_add_u32_e32 v70, s12, v25
	s_lshl_b32 s4, s9, 12
	buffer_load_dwordx4 v[26:29], v68, s[0:3], s4 offen nt
	buffer_load_dwordx4 v[30:33], v67, s[0:3], s4 offen nt
	buffer_load_dwordx4 v[34:37], v69, s[0:3], s4 offen nt
	s_add_i32 s5, s4, 0x10000
	buffer_load_dwordx4 v[38:41], v68, s[0:3], s5 offen nt
	buffer_load_dwordx4 v[42:45], v67, s[0:3], s5 offen nt
	buffer_load_dwordx4 v[16:19], v70, s[0:3], s4 offen nt
	s_add_i32 s10, s4, 0x20000
	buffer_load_dwordx4 v[46:49], v69, s[0:3], s5 offen nt
	buffer_load_dwordx4 v[20:23], v70, s[0:3], s5 offen nt
	s_barrier
	buffer_load_dwordx4 v[50:53], v68, s[0:3], s10 offen nt
	buffer_load_dwordx4 v[54:57], v67, s[0:3], s10 offen nt
	ds_read_b128 v[4:7], v68
	ds_read_b128 v[0:3], v67
	ds_read_b128 v[12:15], v69
	ds_read_b128 v[8:11], v70
	s_add_i32 s5, s4, 0x30000
	v_cmp_gt_u32_e32 vcc, 8, v24
	s_waitcnt vmcnt(9) lgkmcnt(3)
	v_pk_mul_f32 v[28:29], v[6:7], v[28:29]
	v_pk_mul_f32 v[26:27], v[4:5], v[26:27]
	s_waitcnt vmcnt(8) lgkmcnt(2)
	v_pk_fma_f32 v[32:33], v[2:3], v[32:33], v[28:29]
	v_pk_fma_f32 v[30:31], v[0:1], v[30:31], v[26:27]
	buffer_load_dwordx4 v[26:29], v68, s[0:3], s5 offen nt
	s_waitcnt vmcnt(8) lgkmcnt(1)
	v_pk_fma_f32 v[58:59], v[14:15], v[36:37], v[32:33]
	v_pk_fma_f32 v[60:61], v[12:13], v[34:35], v[30:31]
	buffer_load_dwordx4 v[30:33], v67, s[0:3], s5 offen nt
	s_waitcnt vmcnt(8)
	v_pk_mul_f32 v[34:35], v[6:7], v[40:41]
	v_pk_mul_f32 v[36:37], v[4:5], v[38:39]
	s_waitcnt vmcnt(7)
	v_pk_fma_f32 v[44:45], v[2:3], v[44:45], v[34:35]
	v_pk_fma_f32 v[42:43], v[0:1], v[42:43], v[36:37]
	buffer_load_dwordx4 v[34:37], v69, s[0:3], s10 offen nt
	s_waitcnt vmcnt(4)
	v_pk_mul_f32 v[38:39], v[6:7], v[52:53]
	v_pk_mul_f32 v[40:41], v[4:5], v[50:51]
	s_waitcnt vmcnt(3)
	v_pk_fma_f32 v[50:51], v[2:3], v[56:57], v[38:39]
	v_pk_fma_f32 v[52:53], v[0:1], v[54:55], v[40:41]
	buffer_load_dwordx4 v[38:41], v70, s[0:3], s10 offen nt
	v_pk_fma_f32 v[48:49], v[14:15], v[48:49], v[44:45]
	v_pk_fma_f32 v[46:47], v[12:13], v[46:47], v[42:43]
	s_waitcnt lgkmcnt(0)
	v_pk_fma_f32 v[18:19], v[10:11], v[18:19], v[58:59]
	v_pk_fma_f32 v[16:17], v[8:9], v[16:17], v[60:61]
	v_add_f32_e32 v61, v18, v19
	v_add_f32_e32 v60, v16, v17
	v_pk_fma_f32 v[16:17], v[10:11], v[22:23], v[48:49]
	v_pk_fma_f32 v[18:19], v[8:9], v[20:21], v[46:47]
	v_add_f32_e32 v16, v16, v17
	v_add_f32_e32 v18, v18, v19
	v_add_f32_e32 v60, v60, v61
	v_add_f32_e32 v16, v18, v16
	s_add_i32 s10, s4, 0x50000
	s_waitcnt vmcnt(3)
	v_pk_mul_f32 v[28:29], v[6:7], v[28:29]
	v_pk_mul_f32 v[26:27], v[4:5], v[26:27]
	v_add_f32_dpp v16, v16, v16 quad_perm:[1,0,3,2] row_mask:0xf bank_mask:0xf bound_ctrl:1
	s_waitcnt vmcnt(2)
	v_pk_fma_f32 v[54:55], v[2:3], v[32:33], v[28:29]
	v_pk_fma_f32 v[56:57], v[0:1], v[30:31], v[26:27]
	buffer_load_dwordx4 v[26:29], v69, s[0:3], s5 offen nt
	buffer_load_dwordx4 v[30:33], v70, s[0:3], s5 offen nt
	s_add_i32 s5, s4, 0x40000
	buffer_load_dwordx4 v[42:45], v68, s[0:3], s5 offen nt
	s_waitcnt vmcnt(4)
	v_pk_fma_f32 v[50:51], v[14:15], v[36:37], v[50:51]
	v_pk_fma_f32 v[52:53], v[12:13], v[34:35], v[52:53]
	buffer_load_dwordx4 v[34:37], v67, s[0:3], s5 offen nt
	v_add_f32_dpp v16, v16, v16 quad_perm:[2,3,0,1] row_mask:0xf bank_mask:0xf bound_ctrl:1
	s_waitcnt vmcnt(4)
	v_pk_fma_f32 v[58:59], v[10:11], v[40:41], v[50:51]
	v_pk_fma_f32 v[38:39], v[8:9], v[38:39], v[52:53]
	v_add_f32_e32 v19, v58, v59
	v_add_f32_e32 v17, v38, v39
	v_add_f32_dpp v58, v60, v60 quad_perm:[1,0,3,2] row_mask:0xf bank_mask:0xf bound_ctrl:1
	v_add_f32_e32 v18, v17, v19
	v_add_f32_dpp v16, v16, v16 row_ror:4 row_mask:0xf bank_mask:0xf bound_ctrl:1
	v_add_f32_dpp v17, v58, v58 quad_perm:[2,3,0,1] row_mask:0xf bank_mask:0xf bound_ctrl:1
	buffer_load_dwordx4 v[20:23], v69, s[0:3], s5 offen nt
	buffer_load_dwordx4 v[46:49], v70, s[0:3], s5 offen nt
	v_add_f32_dpp v17, v17, v17 row_ror:4 row_mask:0xf bank_mask:0xf bound_ctrl:1
	v_add_f32_dpp v58, v16, v16 row_ror:8 row_mask:0xf bank_mask:0xf bound_ctrl:1
	buffer_load_dwordx4 v[38:41], v67, s[0:3], s10 offen nt
	buffer_load_dwordx4 v[50:53], v68, s[0:3], s10 offen nt
	v_add_f32_dpp v17, v17, v17 row_ror:8 row_mask:0xf bank_mask:0xf bound_ctrl:1
	v_mov_b32_e32 v19, v17
	v_mov_b32_e32 v59, v58
	s_nop 0
	v_permlane16_swap_b32_e32 v17, v19
	v_permlane16_swap_b32_e32 v58, v59
	v_add_f32_e32 v16, v17, v19
	v_add_f32_e32 v17, v58, v59
	s_add_i32 s5, s4, 0x60000
	s_add_i32 s4, s4, 0x70000
	v_add_f32_dpp v18, v18, v18 quad_perm:[1,0,3,2] row_mask:0xf bank_mask:0xf bound_ctrl:1
	s_waitcnt vmcnt(7)
	v_pk_fma_f32 v[28:29], v[14:15], v[28:29], v[54:55]
	v_pk_fma_f32 v[54:55], v[12:13], v[26:27], v[56:57]
	s_waitcnt vmcnt(6)
	v_pk_fma_f32 v[58:59], v[10:11], v[32:33], v[28:29]
	buffer_load_dwordx4 v[26:29], v69, s[0:3], s10 offen nt
	v_pk_fma_f32 v[54:55], v[8:9], v[30:31], v[54:55]
	buffer_load_dwordx4 v[30:33], v70, s[0:3], s10 offen nt
	v_add_f32_e32 v66, v54, v55
	s_waitcnt vmcnt(7)
	v_pk_mul_f32 v[54:55], v[6:7], v[44:45]
	v_pk_mul_f32 v[56:57], v[4:5], v[42:43]
	buffer_load_dwordx4 v[42:45], v68, s[0:3], s5 offen nt
	s_waitcnt vmcnt(7)
	v_pk_fma_f32 v[54:55], v[2:3], v[36:37], v[54:55]
	v_pk_fma_f32 v[56:57], v[0:1], v[34:35], v[56:57]
	buffer_load_dwordx4 v[34:37], v67, s[0:3], s5 offen nt
	v_add_f32_dpp v18, v18, v18 quad_perm:[2,3,0,1] row_mask:0xf bank_mask:0xf bound_ctrl:1
	s_waitcnt vmcnt(7)
	v_pk_fma_f32 v[22:23], v[14:15], v[22:23], v[54:55]
	v_pk_fma_f32 v[20:21], v[12:13], v[20:21], v[56:57]
	s_waitcnt vmcnt(6)
	v_pk_fma_f32 v[60:61], v[10:11], v[48:49], v[22:23]
	v_pk_fma_f32 v[22:23], v[8:9], v[46:47], v[20:21]
	s_waitcnt vmcnt(4)
	v_pk_mul_f32 v[54:55], v[4:5], v[50:51]
	v_pk_mul_f32 v[20:21], v[6:7], v[52:53]
	v_pk_fma_f32 v[38:39], v[0:1], v[38:39], v[54:55]
	buffer_load_dwordx4 v[46:49], v69, s[0:3], s5 offen nt
	buffer_load_dwordx4 v[50:53], v70, s[0:3], s5 offen nt
	v_pk_fma_f32 v[20:21], v[2:3], v[40:41], v[20:21]
	v_add_f32_e32 v23, v22, v23
	v_add_f32_dpp v18, v18, v18 row_ror:4 row_mask:0xf bank_mask:0xf bound_ctrl:1
	s_waitcnt vmcnt(5)
	v_pk_fma_f32 v[26:27], v[12:13], v[26:27], v[38:39]
	buffer_load_dwordx4 v[38:41], v67, s[0:3], s4 offen nt
	buffer_load_dwordx4 v[54:57], v68, s[0:3], s4 offen nt
	v_pk_fma_f32 v[20:21], v[14:15], v[28:29], v[20:21]
	s_waitcnt vmcnt(6)
	v_pk_fma_f32 v[30:31], v[8:9], v[30:31], v[26:27]
	v_pk_fma_f32 v[62:63], v[10:11], v[32:33], v[20:21]
	v_add_f32_dpp v18, v18, v18 row_ror:8 row_mask:0xf bank_mask:0xf bound_ctrl:1
	s_waitcnt vmcnt(5)
	v_pk_mul_f32 v[20:21], v[6:7], v[44:45]
	v_pk_mul_f32 v[26:27], v[4:5], v[42:43]
	buffer_load_dwordx4 v[42:45], v69, s[0:3], s4 offen nt
	s_waitcnt vmcnt(5)
	v_pk_fma_f32 v[64:65], v[0:1], v[34:35], v[26:27]
	buffer_load_dwordx4 v[32:35], v70, s[0:3], s4 offen nt
	v_add_f32_e32 v27, v60, v61
	v_add_f32_e32 v23, v23, v27
	v_pk_fma_f32 v[36:37], v[2:3], v[36:37], v[20:21]
	v_add_f32_e32 v20, v58, v59
	v_add_f32_dpp v23, v23, v23 quad_perm:[1,0,3,2] row_mask:0xf bank_mask:0xf bound_ctrl:1
	v_add_f32_e32 v20, v66, v20
	v_mov_b32_e32 v19, v18
	v_add_f32_dpp v23, v23, v23 quad_perm:[2,3,0,1] row_mask:0xf bank_mask:0xf bound_ctrl:1
	v_add_f32_dpp v20, v20, v20 quad_perm:[1,0,3,2] row_mask:0xf bank_mask:0xf bound_ctrl:1
	v_permlane16_swap_b32_e32 v18, v19
	v_add_f32_dpp v23, v23, v23 row_ror:4 row_mask:0xf bank_mask:0xf bound_ctrl:1
	v_add_f32_dpp v20, v20, v20 quad_perm:[2,3,0,1] row_mask:0xf bank_mask:0xf bound_ctrl:1
	v_add_f32_e32 v18, v18, v19
	v_add_f32_dpp v23, v23, v23 row_ror:8 row_mask:0xf bank_mask:0xf bound_ctrl:1
	v_mov_b32_e32 v27, v23
	s_nop 1
	v_permlane16_swap_b32_e32 v23, v27
	v_add_f32_e32 v28, v23, v27
	v_add_f32_e32 v23, v30, v31
	s_waitcnt vmcnt(5)
	v_pk_fma_f32 v[30:31], v[14:15], v[48:49], v[36:37]
	v_pk_fma_f32 v[36:37], v[12:13], v[46:47], v[64:65]
	s_waitcnt vmcnt(4)
	v_pk_fma_f32 v[30:31], v[10:11], v[52:53], v[30:31]
	v_pk_fma_f32 v[36:37], v[8:9], v[50:51], v[36:37]
	v_add_f32_e32 v27, v62, v63
	v_add_f32_e32 v36, v36, v37
	v_add_f32_e32 v30, v30, v31
	v_add_f32_e32 v23, v23, v27
	v_add_f32_e32 v30, v36, v30
	v_add_f32_dpp v20, v20, v20 row_ror:4 row_mask:0xf bank_mask:0xf bound_ctrl:1
	v_add_f32_dpp v23, v23, v23 quad_perm:[1,0,3,2] row_mask:0xf bank_mask:0xf bound_ctrl:1
	v_add_f32_dpp v30, v30, v30 quad_perm:[1,0,3,2] row_mask:0xf bank_mask:0xf bound_ctrl:1
	v_add_f32_dpp v20, v20, v20 row_ror:8 row_mask:0xf bank_mask:0xf bound_ctrl:1
	v_add_f32_dpp v23, v23, v23 quad_perm:[2,3,0,1] row_mask:0xf bank_mask:0xf bound_ctrl:1
	v_add_f32_dpp v30, v30, v30 quad_perm:[2,3,0,1] row_mask:0xf bank_mask:0xf bound_ctrl:1
	v_mov_b32_e32 v21, v20
	v_add_f32_dpp v23, v23, v23 row_ror:4 row_mask:0xf bank_mask:0xf bound_ctrl:1
	v_add_f32_dpp v30, v30, v30 row_ror:4 row_mask:0xf bank_mask:0xf bound_ctrl:1
	v_permlane16_swap_b32_e32 v20, v21
	v_add_f32_dpp v23, v23, v23 row_ror:8 row_mask:0xf bank_mask:0xf bound_ctrl:1
	v_add_f32_dpp v30, v30, v30 row_ror:8 row_mask:0xf bank_mask:0xf bound_ctrl:1
	v_mov_b32_e32 v27, v23
	v_mov_b32_e32 v31, v30
	s_nop 0
	v_permlane16_swap_b32_e32 v23, v27
	v_permlane16_swap_b32_e32 v30, v31
	v_add_f32_e32 v21, v20, v21
	v_add_f32_e32 v23, v23, v27
	v_add_f32_e32 v30, v30, v31
	v_mov_b32_e32 v19, v16
	v_mov_b32_e32 v20, v17
	v_mov_b32_e32 v22, v18
	v_mov_b32_e32 v26, v21
	v_mov_b32_e32 v29, v28
	v_mov_b32_e32 v27, v23
	v_mov_b32_e32 v31, v30
	v_permlane32_swap_b32_e32 v16, v19
	v_permlane32_swap_b32_e32 v17, v20
	v_permlane32_swap_b32_e32 v18, v22
	v_permlane32_swap_b32_e32 v21, v26
	v_permlane32_swap_b32_e32 v28, v29
	v_permlane32_swap_b32_e32 v23, v27
	s_waitcnt vmcnt(2)
	v_pk_mul_f32 v[6:7], v[6:7], v[56:57]
	v_pk_mul_f32 v[4:5], v[4:5], v[54:55]
	v_pk_fma_f32 v[2:3], v[2:3], v[40:41], v[6:7]
	v_pk_fma_f32 v[0:1], v[0:1], v[38:39], v[4:5]
	v_permlane32_swap_b32_e32 v30, v31
	s_waitcnt vmcnt(1)
	v_pk_fma_f32 v[2:3], v[14:15], v[44:45], v[2:3]
	v_pk_fma_f32 v[0:1], v[12:13], v[42:43], v[0:1]
	s_waitcnt vmcnt(0)
	v_pk_fma_f32 v[2:3], v[10:11], v[34:35], v[2:3]
	v_pk_fma_f32 v[0:1], v[8:9], v[32:33], v[0:1]
	s_nop 0
	v_add_f32_e32 v0, v0, v1
	v_add_f32_e32 v1, v2, v3
	v_add_f32_e32 v0, v0, v1
	s_nop 1
	v_add_f32_dpp v0, v0, v0 quad_perm:[1,0,3,2] row_mask:0xf bank_mask:0xf bound_ctrl:1
	s_nop 1
	v_add_f32_dpp v0, v0, v0 quad_perm:[2,3,0,1] row_mask:0xf bank_mask:0xf bound_ctrl:1
	s_nop 1
	v_add_f32_dpp v0, v0, v0 row_ror:4 row_mask:0xf bank_mask:0xf bound_ctrl:1
	s_nop 1
	v_add_f32_dpp v0, v0, v0 row_ror:8 row_mask:0xf bank_mask:0xf bound_ctrl:1
	v_mov_b32_e32 v1, v0
	s_nop 1
	v_permlane16_swap_b32_e32 v0, v1
	v_add_f32_e32 v0, v0, v1
	v_mov_b32_e32 v1, v0
	s_nop 1
	v_permlane32_swap_b32_e32 v0, v1
	s_and_saveexec_b64 s[0:1], vcc
	s_cbranch_execz .LBB1_4
	v_add_f32_e32 v6, v16, v19
	v_cmp_eq_u32_e32 vcc, 0, v24
	v_add_f32_e32 v5, v17, v20
	v_add_f32_e32 v4, v18, v22
	v_cndmask_b32_e32 v6, 0, v6, vcc
	v_cmp_eq_u32_e32 vcc, 1, v24
	v_add_f32_e32 v3, v21, v26
	v_add_f32_e32 v2, v28, v29
	v_cndmask_b32_e32 v5, v6, v5, vcc
	v_cmp_eq_u32_e32 vcc, 2, v24
	v_add_f32_e32 v0, v0, v1
	v_add_f32_e32 v1, v30, v31
	v_cndmask_b32_e32 v4, v5, v4, vcc
	v_cmp_eq_u32_e32 vcc, 3, v24
	s_lshl_b32 s0, s8, 13
	s_and_b32 s0, s0, 0x1e000
	v_cndmask_b32_e32 v3, v4, v3, vcc
	v_cmp_eq_u32_e32 vcc, 4, v24
	s_add_u32 s0, s6, s0
	s_addc_u32 s1, s7, 0
	v_cndmask_b32_e32 v2, v3, v2, vcc
	v_add_f32_e32 v3, v23, v27
	v_cmp_eq_u32_e32 vcc, 5, v24
	s_nop 1
	v_cndmask_b32_e32 v2, v2, v3, vcc
	v_cmp_eq_u32_e32 vcc, 6, v24
	s_nop 1
	v_cndmask_b32_e32 v1, v2, v1, vcc
	v_cmp_eq_u32_e32 vcc, 7, v24
	s_nop 1
	v_cndmask_b32_e32 v2, v1, v0, vcc
	v_add_u32_e32 v0, s9, v25
	v_ashrrev_i32_e32 v0, 4, v0
	v_ashrrev_i32_e32 v1, 31, v0
	v_lshl_add_u64 v[0:1], v[0:1], 2, s[0:1]
	v_add_co_u32_e32 v0, vcc, 0x6000, v0
	s_nop 1
	v_addc_co_u32_e32 v1, vcc, 0, v1, vcc
	global_store_dword v[0:1], v2, off offset:64
